# speedup vs baseline: 1.0133x; 1.0133x over previous
.Lskip_late_sleep:
	v_bfe_u32 v41, v0, 5, 1
	v_and_b32_e32 v40, 31, v0
	s_lshl_b32 s0, s2, 10
	v_lshlrev_b32_e32 v1, 9, v41
	v_or3_b32 v1, v1, s0, v40
	s_waitcnt lgkmcnt(0)
	s_and_b32 s13, s7, 0xffff
	s_mov_b32 s15, 0x20000
	s_mov_b32 s14, 0x200000
	s_mov_b32 s12, s6
	v_lshlrev_b32_e32 v1, 2, v1
	buffer_load_dword v18, v1, s[12:15], 0 offen nt
	buffer_load_dword v19, v1, s[12:15], 0 offen offset:128 nt
	buffer_load_dword v20, v1, s[12:15], 0 offen offset:256 nt
	buffer_load_dword v21, v1, s[12:15], 0 offen offset:384 nt
	buffer_load_dword v22, v1, s[12:15], 0 offen offset:512 nt
	buffer_load_dword v23, v1, s[12:15], 0 offen offset:640 nt
	buffer_load_dword v24, v1, s[12:15], 0 offen offset:768 nt
	buffer_load_dword v25, v1, s[12:15], 0 offen offset:896 nt
	buffer_load_dword v26, v1, s[12:15], 0 offen offset:1024 nt
	buffer_load_dword v27, v1, s[12:15], 0 offen offset:1152 nt
	buffer_load_dword v28, v1, s[12:15], 0 offen offset:1280 nt
	buffer_load_dword v29, v1, s[12:15], 0 offen offset:1408 nt
	buffer_load_dword v30, v1, s[12:15], 0 offen offset:1536 nt
	buffer_load_dword v31, v1, s[12:15], 0 offen offset:1664 nt
	buffer_load_dword v32, v1, s[12:15], 0 offen offset:1792 nt
	s_nop 0
	buffer_load_dword v1, v1, s[12:15], 0 offen offset:1920 nt
	v_lshrrev_b32_e32 v42, 6, v0
	s_lshl_b32 s0, s2, 5
	v_lshlrev_b32_e32 v3, 2, v0
	v_lshl_add_u32 v2, v42, 19, s0
	v_and_b32_e32 v34, 28, v3
	v_or_b32_e32 v2, v2, v34
	v_bfe_u32 v33, v0, 3, 3
	v_lshlrev_b32_e32 v2, 2, v2
	s_and_b32 s5, s5, 0xffff
	s_mov_b32 s6, 0x800000
	s_mov_b32 s7, s15
	s_and_b32 s9, s9, 0xffff
	s_mov_b32 s10, s6
	s_mov_b32 s11, s15
	s_mov_b32 s16, 0x80000
	s_mov_b32 s17, 0x100000
	s_mov_b32 s18, 0x180000
	v_lshl_add_u32 v35, v33, 16, v2
	v_mov_b32_e32 v60, v35
	s_mov_b32 s0, 0x80000
	buffer_load_dwordx4 v[2:5], v35, s[4:7], 0 offen nt
	buffer_load_dwordx4 v[6:9], v35, s[4:7], s0 offen nt
	s_mov_b32 s0, 0x100000
	s_mov_b32 s1, 0x180000
	buffer_load_dwordx4 v[10:13], v35, s[4:7], s0 offen nt
	buffer_load_dwordx4 v[14:17], v35, s[4:7], s1 offen nt
	v_and_b32_e32 v35, 63, v0
	s_waitcnt vmcnt(18)
	v_max_f32_e32 v0, v19, v19
	v_max_f32_e32 v36, v18, v18
	v_max_f32_e32 v0, v36, v0
	s_waitcnt vmcnt(16)
	v_max3_f32 v0, v0, v20, v21
	s_waitcnt vmcnt(14)
	v_max3_f32 v0, v0, v22, v23
	s_waitcnt vmcnt(12)
	v_max3_f32 v0, v0, v24, v25
	s_waitcnt vmcnt(10)
	v_max3_f32 v0, v0, v26, v27
	s_waitcnt vmcnt(8)
	v_max3_f32 v0, v0, v28, v29
	s_waitcnt vmcnt(6)
	v_max3_f32 v0, v0, v30, v31
	s_waitcnt vmcnt(4)
	v_max3_f32 v0, v0, v32, v1
	v_mov_b32_e32 v36, v0
	s_nop 1
	v_permlane32_swap_b32_e32 v0, v36
	v_max_f32_e32 v36, v36, v36
	v_max_f32_e32 v0, v0, v0
	v_max_f32_e32 v0, v0, v36
	v_mov_b32_e32 v36, 0xc1600000
	s_mov_b32 s0, 0x3fb8aa3b
	v_fmamk_f32 v0, v0, 0x3fb8aa3b, v36
	v_fma_f32 v18, v18, s0, -v0
	v_exp_f32_e32 v37, v18
	v_fma_f32 v18, v19, s0, -v0
	v_exp_f32_e32 v38, v18
	v_fma_f32 v18, v20, s0, -v0
	v_exp_f32_e32 v20, v18
	v_fma_f32 v18, v21, s0, -v0
	v_exp_f32_e32 v21, v18
	v_fma_f32 v19, v22, s0, -v0
	v_add_f32_e32 v18, 0, v37
	v_exp_f32_e32 v22, v19
	v_fma_f32 v19, v23, s0, -v0
	v_add_f32_e32 v18, v18, v38
	v_exp_f32_e32 v39, v19
	v_fma_f32 v19, v24, s0, -v0
	v_add_f32_e32 v18, v18, v20
	v_exp_f32_e32 v23, v19
	v_fma_f32 v19, v25, s0, -v0
	v_add_f32_e32 v18, v18, v21
	v_exp_f32_e32 v24, v19
	v_fma_f32 v19, v26, s0, -v0
	v_add_f32_e32 v18, v18, v22
	v_exp_f32_e32 v43, v19
	v_fma_f32 v19, v27, s0, -v0
	v_add_f32_e32 v18, v18, v39
	v_exp_f32_e32 v44, v19
	v_fma_f32 v19, v28, s0, -v0
	v_add_f32_e32 v18, v18, v23
	v_exp_f32_e32 v45, v19
	v_fma_f32 v19, v29, s0, -v0
	v_add_f32_e32 v18, v18, v24
	v_exp_f32_e32 v46, v19
	v_fma_f32 v19, v30, s0, -v0
	v_add_f32_e32 v18, v18, v43
	v_exp_f32_e32 v47, v19
	v_fma_f32 v19, v31, s0, -v0
	v_add_f32_e32 v18, v18, v44
	v_exp_f32_e32 v48, v19
	v_fma_f32 v19, v32, s0, -v0
	v_add_f32_e32 v18, v18, v45
	v_exp_f32_e32 v49, v19
	v_fma_f32 v0, v1, s0, -v0
	v_add_f32_e32 v18, v18, v46
	v_exp_f32_e32 v50, v0
	v_add_f32_e32 v0, v18, v47
	v_add_f32_e32 v0, v0, v48
	v_add_f32_e32 v0, v0, v49
	v_add_f32_e32 v0, v0, v50
	v_mov_b32_e32 v1, v0
	s_nop 1
	v_permlane32_swap_b32_e32 v0, v1
	v_add_f32_e32 v0, v0, v1
	v_log_f32_e32 v0, v0
	s_nop 0
	v_add_f32_e32 v0, 0x41600000, v0
	v_mul_f32_e32 v25, 0xbf317218, v0
	v_mul_u32_u24_e32 v0, 0x1200, v42
	v_mul_u32_u24_e32 v1, 0x90, v33
	v_lshlrev_b32_e32 v18, 2, v34
	v_add3_u32 v1, v0, v1, v18
	v_mov_b32_e32 v59, v1
	s_waitcnt vmcnt(3)
	ds_write_b128 v1, v[2:5]
	s_waitcnt vmcnt(2)
	ds_write_b128 v1, v[6:9] offset:1152
	s_waitcnt vmcnt(1)
	ds_write_b128 v1, v[10:13] offset:2304
	s_waitcnt vmcnt(0)
	ds_write_b128 v1, v[14:17] offset:3456
	v_mul_u32_u24_e32 v1, 0x90, v40
	v_lshlrev_b32_e32 v2, 6, v41
	v_add3_u32 v12, v0, v1, v2
	v_lshlrev_b32_e32 v58, 4, v41
	v_add3_u32 v57, v0, v1, v58
	ds_read_b128 v[0:3], v12
	ds_read_b128 v[4:7], v12 offset:16
	ds_read_b128 v[8:11], v12 offset:32
	ds_read_b128 v[16:19], v12 offset:48
	v_cmp_gt_u32_e32 vcc, 32, v35
	s_waitcnt lgkmcnt(3)
	v_max_f32_e32 v12, v1, v1
	v_max_f32_e32 v13, v0, v0
	v_max_f32_e32 v12, v13, v12
	v_max3_f32 v12, v12, v2, v3
	s_waitcnt lgkmcnt(2)
	v_max3_f32 v12, v12, v4, v5
	v_max3_f32 v12, v12, v6, v7
	s_waitcnt lgkmcnt(1)
	v_max3_f32 v12, v12, v8, v9
	v_max3_f32 v12, v12, v10, v11
	s_waitcnt lgkmcnt(0)
	v_max3_f32 v12, v12, v16, v17
	v_max3_f32 v12, v12, v18, v19
	v_mov_b32_e32 v13, v12
	s_nop 1
	v_permlane32_swap_b32_e32 v12, v13
	v_max_f32_e32 v13, v13, v13
	v_max_f32_e32 v12, v12, v12
	v_max_f32_e32 v12, v12, v13
	v_fmac_f32_e32 v36, 0x3fb8aa3b, v12
	v_fma_f32 v0, v0, s0, -v36
	v_cndmask_b32_e64 v13, v25, 1.0, vcc
	v_exp_f32_e32 v25, v0
	v_fma_f32 v0, v1, s0, -v36
	v_exp_f32_e32 v26, v0
	v_fma_f32 v0, v2, s0, -v36
	v_exp_f32_e32 v27, v0
	v_fma_f32 v0, v3, s0, -v36
	v_exp_f32_e32 v28, v0
	v_fma_f32 v0, v4, s0, -v36
	v_exp_f32_e32 v29, v0
	v_fma_f32 v0, v5, s0, -v36
	v_exp_f32_e32 v30, v0
	v_fma_f32 v0, v6, s0, -v36
	v_exp_f32_e32 v31, v0
	v_fma_f32 v0, v7, s0, -v36
	v_exp_f32_e32 v32, v0
	v_fma_f32 v16, v16, s0, -v36
	v_fma_f32 v0, v8, s0, -v36
	v_exp_f32_e32 v34, v16
	v_fma_f32 v16, v17, s0, -v36
	v_exp_f32_e32 v51, v0
	v_fma_f32 v0, v9, s0, -v36
	v_exp_f32_e32 v54, v16
	v_fma_f32 v16, v18, s0, -v36
	v_exp_f32_e32 v52, v0
	v_fma_f32 v0, v10, s0, -v36
	v_exp_f32_e32 v35, v16
	v_fma_f32 v16, v19, s0, -v36
	v_exp_f32_e32 v33, v0
	v_fma_f32 v0, v11, s0, -v36
	v_exp_f32_e32 v36, v16
	v_cvt_pk_f16_f32 v19, v31, v32
	v_cvt_pk_f16_f32 v18, v29, v30
	v_cvt_pk_f16_f32 v17, v27, v28
	v_cvt_pk_f16_f32 v16, v25, v26
	v_cndmask_b32_e32 v1, 1.0, v12, vcc
	v_exp_f32_e32 v53, v0
	v_cvt_pk_f16_f32 v23, v23, v24
	v_cvt_pk_f16_f32 v22, v22, v39
	v_cvt_pk_f16_f32 v21, v20, v21
	v_cvt_pk_f16_f32 v20, v37, v38
	v_cvt_pk_f16_f32 v35, v35, v36
	v_cvt_pk_f16_f32 v34, v34, v54
	v_mfma_f32_32x32x16_f16 v[16:31], v[20:23], v[16:19], 0
	v_cvt_pk_f16_f32 v33, v33, v53
	v_cvt_pk_f16_f32 v32, v51, v52
	v_cvt_pk_f16_f32 v39, v49, v50
	v_cvt_pk_f16_f32 v38, v47, v48
	v_cvt_pk_f16_f32 v37, v45, v46
	v_cvt_pk_f16_f32 v36, v43, v44
	v_mfma_f32_32x32x2_f32 v[0:15], v13, v1, 0
	v_mfma_f32_32x32x16_f16 v[16:31], v[36:39], v[32:35], v[16:31]
	s_mov_b32 s1, 0x3f317218
	s_nop 10
	v_log_f32_e32 v16, v16
	v_log_f32_e32 v17, v17
	v_log_f32_e32 v18, v18
	v_log_f32_e32 v19, v19
	v_log_f32_e32 v20, v20
	v_log_f32_e32 v21, v21
	v_log_f32_e32 v22, v22
	v_log_f32_e32 v23, v23
	v_fmac_f32_e32 v0, s1, v16
	v_fmac_f32_e32 v1, s1, v17
	v_fmac_f32_e32 v2, s1, v18
	v_fmac_f32_e32 v3, s1, v19
	ds_write_b128 v57, v[0:3]
	v_log_f32_e32 v24, v24
	v_log_f32_e32 v25, v25
	v_log_f32_e32 v26, v26
	v_log_f32_e32 v27, v27
	v_fmac_f32_e32 v4, s1, v20
	v_fmac_f32_e32 v5, s1, v21
	v_fmac_f32_e32 v6, s1, v22
	v_fmac_f32_e32 v7, s1, v23
	ds_write_b128 v57, v[4:7] offset:32
	v_log_f32_e32 v28, v28
	v_log_f32_e32 v29, v29
	v_log_f32_e32 v30, v30
	v_log_f32_e32 v31, v31
	v_fmac_f32_e32 v8, s1, v24
	v_fmac_f32_e32 v9, s1, v25
	v_fmac_f32_e32 v10, s1, v26
	v_fmac_f32_e32 v11, s1, v27
	ds_write_b128 v57, v[8:11] offset:64
	v_fmac_f32_e32 v12, s1, v28
	v_fmac_f32_e32 v13, s1, v29
	v_fmac_f32_e32 v14, s1, v30
	v_fmac_f32_e32 v15, s1, v31
	ds_write_b128 v57, v[12:15] offset:96
	ds_read_b128 v[16:19], v59
	ds_read_b128 v[20:23], v59 offset:1152
	ds_read_b128 v[24:27], v59 offset:2304
	ds_read_b128 v[28:31], v59 offset:3456
	s_waitcnt lgkmcnt(3)
	buffer_store_dwordx4 v[16:19], v60, s[8:11], 0 offen sc1
	s_waitcnt lgkmcnt(2)
	buffer_store_dwordx4 v[20:23], v60, s[8:11], s16 offen sc1
	s_waitcnt lgkmcnt(1)
	buffer_store_dwordx4 v[24:27], v60, s[8:11], s17 offen sc1
	s_waitcnt lgkmcnt(0)
	buffer_store_dwordx4 v[28:31], v60, s[8:11], s18 offen sc1
	s_endpgm
